# stack18
# baseline (speedup 1.0000x reference)
_Z7k_gemm2PK15HIP_vector_typeIjLj4EEPKS_IjLj2EEPKfS2_S2_S7_PtS8_:
	s_load_dwordx8 s[12:19], s[0:1], 0x0
	s_load_dwordx8 s[4:11], s[0:1], 0x20
	v_lshlrev_b32_e32 v2, 4, v0
	s_waitcnt lgkmcnt(0)
	s_lshl_b32 s1, s2, 10
	s_bfe_i32 s0, s2, 0x140002
	s_mov_b64 s[20:21], s[18:19]
	global_load_dwordx4 v[8:11], v2, s[20:21]
	s_add_u32 s20, s20, 0x4000
	s_addc_u32 s21, s21, 0
	global_load_dwordx4 v[12:15], v2, s[20:21]
	s_add_u32 s20, s20, 0x4000
	s_addc_u32 s21, s21, 0
	global_load_dwordx4 v[16:19], v2, s[20:21]
	s_add_u32 s20, s20, 0x4000
	s_addc_u32 s21, s21, 0
	global_load_dwordx4 v[20:23], v2, s[20:21]
	s_add_u32 s20, s20, 0x4000
	s_addc_u32 s21, s21, 0
	global_load_dwordx4 v[24:27], v2, s[20:21]
	s_add_u32 s20, s20, 0x4000
	s_addc_u32 s21, s21, 0
	global_load_dwordx4 v[28:31], v2, s[20:21]
	s_add_u32 s20, s20, 0x4000
	s_addc_u32 s21, s21, 0
	s_add_u32 s22, s4, 0x13000
	s_addc_u32 s23, s5, 0
	global_load_dwordx4 v[32:35], v2, s[22:23]
	v_cmp_gt_u32_e32 vcc, 0x100, v0
	s_and_saveexec_b64 s[24:25], vcc
	global_load_dwordx4 v[36:39], v2, s[20:21]
	s_mov_b64 exec, s[24:25]
	v_cmp_gt_u32_e32 vcc, 0x200, v0
	s_add_u32 s22, s22, 0x4000
	s_addc_u32 s23, s23, 0
	s_and_saveexec_b64 s[24:25], vcc
	global_load_dwordx4 v[40:43], v2, s[22:23]
	s_mov_b64 exec, s[24:25]
	v_cmp_gt_u32_e32 vcc, 0x64, v0
	s_mul_i32 s26, s0, 0x190
	s_add_u32 s22, s16, s26
	s_addc_u32 s23, s17, 0
	v_lshlrev_b32_e32 v3, 2, v0
	s_and_saveexec_b64 s[24:25], vcc
	global_load_dword v44, v3, s[22:23]
	s_mov_b64 exec, s[24:25]
	v_add_u32_e32 v4, 0x10000, v2
	v_add_u32_e32 v5, 0x19000, v2
	v_mov_b32_e32 v6, 0x1f000
	v_lshl_or_b32 v6, v0, 2, v6
	s_waitcnt vmcnt(0)
	ds_write_b128 v2, v[8:11]
	ds_write_b128 v2, v[12:15] offset:16384
	ds_write_b128 v2, v[16:19] offset:32768
	ds_write_b128 v2, v[20:23] offset:49152
	ds_write_b128 v4, v[24:27]
	ds_write_b128 v4, v[28:31] offset:16384
	ds_write_b128 v5, v[32:35]
	v_cmp_gt_u32_e32 vcc, 0x100, v0
	s_and_saveexec_b64 s[24:25], vcc
	ds_write_b128 v4, v[36:39] offset:32768
	s_mov_b64 exec, s[24:25]
	v_cmp_gt_u32_e32 vcc, 0x200, v0
	s_and_saveexec_b64 s[24:25], vcc
	ds_write_b128 v5, v[40:43] offset:16384
	s_mov_b64 exec, s[24:25]
	v_cmp_gt_u32_e32 vcc, 0x64, v0
	s_and_saveexec_b64 s[24:25], vcc
	ds_write_b32 v6, v44
	s_mov_b64 exec, s[24:25]
	v_mov_b32_e32 v1, 0xfc0
	v_bfe_u32 v97, v0, 5, 1
	v_bitop3_b32 v98, s1, v1, v0 bitop3:0xc8
	s_mul_i32 s1, s0, 24
	v_and_b32_e32 v96, 31, v0
	v_or_b32_e32 v0, s1, v97
	v_ashrrev_i32_e32 v1, 31, v0
	v_lshlrev_b64 v[0:1], 16, v[0:1]
	v_lshl_add_u64 v[0:1], s[12:13], 0, v[0:1]
	v_mov_b32_e32 v49, 0
	v_lshlrev_b32_e32 v48, 4, v98
	v_lshl_add_u64 v[0:1], v[0:1], 0, v[48:49]
	v_lshlrev_b32_e32 v48, 4, v96
	v_lshl_add_u64 v[100:101], v[0:1], 0, v[48:49]
	s_mov_b64 s[2:3], 0x160000
	v_lshl_add_u64 v[0:1], v[100:101], 0, s[2:3]
	s_mov_b64 s[2:3], 0x160200
	global_load_dwordx4 v[72:75], v[0:1], off
	v_lshl_add_u64 v[0:1], v[100:101], 0, s[2:3]
	s_mov_b64 s[2:3], 0x140000
	global_load_dwordx4 v[64:67], v[0:1], off
	v_lshl_add_u64 v[0:1], v[100:101], 0, s[2:3]
	s_mov_b64 s[2:3], 0x140200
	global_load_dwordx4 v[76:79], v[0:1], off
	v_lshl_add_u64 v[0:1], v[100:101], 0, s[2:3]
	v_lshlrev_b32_e32 v99, 2, v97
	v_lshl_or_b32 v102, v97, 10, v48
	global_load_dwordx4 v[68:71], v[0:1], off
	s_waitcnt lgkmcnt(0)
	s_barrier
	s_mov_b32 s2, -2
	s_mov_b32 s3, 0
	s_mov_b64 s[4:5], 0x200
	v_mov_b32_e32 v103, v102
	v_mov_b32_e32 v104, v99
	v_mov_b32_e32 v48, v49
	v_mov_b32_e32 v50, v49
	v_mov_b32_e32 v51, v49
	v_mov_b32_e32 v52, v49
	v_mov_b32_e32 v53, v49
	v_mov_b32_e32 v54, v49
	v_mov_b32_e32 v55, v49
	v_mov_b32_e32 v56, v49
	v_mov_b32_e32 v57, v49
	v_mov_b32_e32 v58, v49
	v_mov_b32_e32 v59, v49
	v_mov_b32_e32 v60, v49
	v_mov_b32_e32 v61, v49
	v_mov_b32_e32 v62, v49
	v_mov_b32_e32 v63, v49
	v_mov_b32_e32 v32, v49
	v_mov_b32_e32 v33, v49
	v_mov_b32_e32 v34, v49
	v_mov_b32_e32 v35, v49
	v_mov_b32_e32 v36, v49
	v_mov_b32_e32 v37, v49
	v_mov_b32_e32 v38, v49
	v_mov_b32_e32 v39, v49
	v_mov_b32_e32 v40, v49
	v_mov_b32_e32 v41, v49
	v_mov_b32_e32 v42, v49
	v_mov_b32_e32 v43, v49
	v_mov_b32_e32 v44, v49
	v_mov_b32_e32 v45, v49
	v_mov_b32_e32 v46, v49
	v_mov_b32_e32 v47, v49
	v_mov_b32_e32 v16, v49
	v_mov_b32_e32 v17, v49
	v_mov_b32_e32 v18, v49
	v_mov_b32_e32 v19, v49
	v_mov_b32_e32 v20, v49
	v_mov_b32_e32 v21, v49
	v_mov_b32_e32 v22, v49
	v_mov_b32_e32 v23, v49
	v_mov_b32_e32 v24, v49
	v_mov_b32_e32 v25, v49
	v_mov_b32_e32 v26, v49
	v_mov_b32_e32 v27, v49
	v_mov_b32_e32 v28, v49
	v_mov_b32_e32 v29, v49
	v_mov_b32_e32 v30, v49
	v_mov_b32_e32 v31, v49
	v_mov_b32_e32 v0, v49
	v_mov_b32_e32 v1, v49
	v_mov_b32_e32 v2, v49
	v_mov_b32_e32 v3, v49
	v_mov_b32_e32 v4, v49
	v_mov_b32_e32 v5, v49
	v_mov_b32_e32 v6, v49
	v_mov_b32_e32 v7, v49
	v_mov_b32_e32 v8, v49
	v_mov_b32_e32 v9, v49
	v_mov_b32_e32 v10, v49
	v_mov_b32_e32 v11, v49
	v_mov_b32_e32 v12, v49
	v_mov_b32_e32 v13, v49
	v_mov_b32_e32 v14, v49
	v_mov_b32_e32 v15, v49
